# E phase: fp16 residual rows stored write-back (plain) instead of write-through; consumed only next layer
# speedup vs baseline: 1.0019x; 1.0019x over previous
; __device__ void phase_E_rows(const Params& p, int l, char* smem, int vb, int nvb, bool split, int nrows, int oz) {
;     ...
;         float ss2 = 0.f;
; #pragma unroll
;         for (int k = 0; k < 4; ++k) {
;             if (l > 0) {
;                 xv[k].x += gp[k].x * (y[k][0] * rs);
;                 xv[k].y += gp[k].y * (y[k][1] * rs);
;                 xv[k].z += gp[k].z * (y[k][2] * rs);
;                 xv[k].w += gp[k].w * (y[k][3] * rs);
;             }
;             ss2 += xv[k].x * xv[k].x + xv[k].y * xv[k].y + xv[k].z * xv[k].z + xv[k].w * xv[k].w;
;         }
;         if (l > 0) {
;             const __amdgpu_buffer_rsrc_t xr = __builtin_amdgcn_make_buffer_rsrc((void*)xcur, (short)0, 4096, 0x00020000);
; #pragma unroll
;             for (int k2 = 0; k2 < 2; ++k2) {
;                 const u32x4 xb = {pk_h2(xv[2 * k2].x, xv[2 * k2].y), pk_h2(xv[2 * k2].z, xv[2 * k2].w), pk_h2(xv[2 * k2 + 1].x, xv[2 * k2 + 1].y), pk_h2(xv[2 * k2 + 1].z, xv[2 * k2 + 1].w)};
;                 __builtin_amdgcn_raw_buffer_store_b128(xb, xr, 2048 + (k2 * 512 + lane * 8) * 2, 0, 16);
;             }
;         }
.LBB0_960:
	v_cvt_f32_f16_e32 v47, v25
	v_cvt_f32_f16_sdwa v25, v25 dst_sel:DWORD dst_unused:UNUSED_PAD src0_sel:WORD_1
	v_cvt_f32_f16_e32 v107, v24
	v_cvt_f32_f16_sdwa v109, v24 dst_sel:DWORD dst_unused:UNUSED_PAD src0_sel:WORD_1
	v_cndmask_b32_e64 v24, v47, v42, s[38:39]
	v_cndmask_b32_e64 v25, v25, v43, s[38:39]
	v_cvt_f32_f16_e32 v42, v27
	v_cvt_f32_f16_sdwa v27, v27 dst_sel:DWORD dst_unused:UNUSED_PAD src0_sel:WORD_1
	v_cvt_f32_f16_e32 v43, v26
	v_cvt_f32_f16_sdwa v26, v26 dst_sel:DWORD dst_unused:UNUSED_PAD src0_sel:WORD_1
	v_cndmask_b32_e64 v40, v107, v40, s[38:39]
	v_cndmask_b32_e64 v39, v27, v39, s[38:39]
	v_cvt_f32_f16_e32 v27, v20
	v_cndmask_b32_e64 v37, v26, v37, s[38:39]
	v_cvt_f32_f16_e32 v26, v21
	v_cvt_f32_f16_sdwa v21, v21 dst_sel:DWORD dst_unused:UNUSED_PAD src0_sel:WORD_1
	v_cvt_f32_f16_sdwa v20, v20 dst_sel:DWORD dst_unused:UNUSED_PAD src0_sel:WORD_1
	v_cndmask_b32_e64 v41, v109, v41, s[38:39]
	v_cndmask_b32_e64 v38, v42, v38, s[38:39]
	v_cndmask_b32_e64 v35, v21, v35, s[38:39]
	v_cndmask_b32_e64 v33, v20, v33, s[38:39]
	v_cvt_f32_f16_e32 v20, v23
	v_cvt_f32_f16_sdwa v21, v23 dst_sel:DWORD dst_unused:UNUSED_PAD src0_sel:WORD_1
	v_cvt_f32_f16_e32 v23, v22
	v_cvt_f32_f16_sdwa v22, v22 dst_sel:DWORD dst_unused:UNUSED_PAD src0_sel:WORD_1
	v_cndmask_b32_e64 v36, v43, v36, s[38:39]
	v_cndmask_b32_e64 v42, v20, v30, s[38:39]
	v_cndmask_b32_e64 v43, v21, v31, s[38:39]
	v_pk_mul_f32 v[20:21], v[46:47], v[174:175] op_sel_hi:[0,1]
	v_cndmask_b32_e64 v176, v23, v28, s[38:39]
	v_cndmask_b32_e64 v177, v22, v29, s[38:39]
	v_pk_fma_f32 v[22:23], v[118:119], v[20:21], v[40:41]
	v_pk_mul_f32 v[20:21], v[46:47], v[172:173] op_sel_hi:[0,1]
	v_cndmask_b32_e64 v34, v26, v34, s[38:39]
	v_cndmask_b32_e64 v32, v27, v32, s[38:39]
	v_pk_fma_f32 v[20:21], v[120:121], v[20:21], v[24:25]
	v_cndmask_b32_e64 v27, v41, v23, s[36:37]
	v_cndmask_b32_e64 v26, v40, v22, s[36:37]
	v_pk_mul_f32 v[22:23], v[46:47], v[170:171] op_sel_hi:[0,1]
	v_cndmask_b32_e64 v21, v25, v21, s[36:37]
	v_cndmask_b32_e64 v20, v24, v20, s[36:37]
	v_pk_fma_f32 v[24:25], v[122:123], v[22:23], v[36:37]
	v_pk_mul_f32 v[22:23], v[46:47], v[168:169] op_sel_hi:[0,1]
	v_cndmask_b32_e64 v31, v37, v25, s[36:37]
	v_cndmask_b32_e64 v30, v36, v24, s[36:37]
	v_pk_mul_f32 v[24:25], v[46:47], v[166:167] op_sel_hi:[0,1]
	v_pk_fma_f32 v[28:29], v[126:127], v[24:25], v[32:33]
	v_pk_mul_f32 v[24:25], v[46:47], v[50:51] op_sel_hi:[0,1]
	v_pk_fma_f32 v[24:25], v[128:129], v[24:25], v[34:35]
	v_cndmask_b32_e64 v33, v33, v29, s[36:37]
	v_cndmask_b32_e64 v32, v32, v28, s[36:37]
	v_pk_mul_f32 v[28:29], v[46:47], v[48:49] op_sel_hi:[0,1]
	v_cndmask_b32_e64 v25, v35, v25, s[36:37]
	v_cndmask_b32_e64 v24, v34, v24, s[36:37]
	v_pk_fma_f32 v[34:35], v[134:135], v[28:29], v[176:177]
	v_pk_mul_f32 v[28:29], v[46:47], v[44:45] op_sel_hi:[0,1]
	v_pk_fma_f32 v[22:23], v[124:125], v[22:23], v[38:39]
	v_pk_fma_f32 v[28:29], v[136:137], v[28:29], v[42:43]
	v_cndmask_b32_e64 v23, v39, v23, s[36:37]
	v_cndmask_b32_e64 v22, v38, v22, s[36:37]
	v_cndmask_b32_e64 v29, v43, v29, s[36:37]
	v_cndmask_b32_e64 v28, v42, v28, s[36:37]
	v_cndmask_b32_e64 v35, v177, v35, s[36:37]
	s_and_b64 vcc, exec, s[44:45]
	v_cndmask_b32_e64 v34, v176, v34, s[36:37]
	s_cbranch_vccnz .LBB0_962
	s_add_i32 s28, s56, 0xffffc000
	s_and_b64 s[20:21], s[20:21], exec
	v_readlane_b32 s4, v253, 18
	s_cselect_b32 s21, 0, s57
	s_cselect_b32 s20, s28, s56
	v_readlane_b32 s18, v253, 32
	v_readlane_b32 s19, v253, 33
	s_cselect_b32 s28, s95, s19
	s_cselect_b32 s29, s94, s18
	s_lshl_b64 s[20:21], s[20:21], 12
	s_add_u32 s20, s29, s20
	s_addc_u32 s21, s28, s21
	s_and_b32 s21, s21, 0xffff
	v_cvt_pk_f16_f32 v36, v26, v27
	v_cvt_pk_f16_f32 v37, v20, v21
	v_cvt_pk_f16_f32 v38, v30, v31
	v_cvt_pk_f16_f32 v39, v22, v23
	s_mov_b64 s[18:19], s[88:89]
	buffer_store_dwordx4 v[36:39], v1, s[20:23], 0 offen
	v_readlane_b32 s5, v253, 19
	v_readlane_b32 s6, v253, 20
	v_cvt_pk_f16_f32 v36, v32, v33
	v_cvt_pk_f16_f32 v37, v24, v25
	v_cvt_pk_f16_f32 v38, v34, v35
	v_cvt_pk_f16_f32 v39, v28, v29
	v_readlane_b32 s7, v253, 21
	v_readlane_b32 s8, v253, 22
	v_readlane_b32 s9, v253, 23
	v_readlane_b32 s10, v253, 24
	v_readlane_b32 s11, v253, 25
	v_readlane_b32 s12, v253, 26
	v_readlane_b32 s13, v253, 27
	v_readlane_b32 s14, v253, 28
	v_readlane_b32 s15, v253, 29
	v_readlane_b32 s16, v253, 30
	v_readlane_b32 s17, v253, 31
	buffer_store_dwordx4 v[36:39], v101, s[20:23], 0 offen
